# best + P9: each wave touches 64 lines of the next unit's weight tile at epilogue start (8 sharers cover the whole 512KB tile) as an L2/MALL prefetch
# speedup vs baseline: 1.0042x; 1.0042x over previous
; #define LAS __attribute__((address_space(3)))
; DI f32x2 swiglu4_2(f32x2 hg, f32x2 hl) {
;     f32x2 glu, lin, ex, sg;
;     glu[0] = fminf(hg[0], 7.0f); glu[1] = fminf(hg[1], 7.0f); lin[0] = __builtin_amdgcn_fmed3f(hl[0], -7.0f, 7.0f); lin[1] = __builtin_amdgcn_fmed3f(hl[1], -7.0f, 7.0f);
;     const f32x2 t = glu * (-1.702f * 1.4426950408889634f);
;     ex[0] = __builtin_amdgcn_exp2f(t[0]); ex[1] = __builtin_amdgcn_exp2f(t[1]);
;     const f32x2 den = ex + 1.0f;
;     sg[0] = __builtin_amdgcn_rcpf(den[0]); sg[1] = __builtin_amdgcn_rcpf(den[1]);
;     return (glu * sg) * (lin * 4.0f + 4.0f);
; }
;     DI void operator()(const f32x4 (&acc)[2][2][4][2], const Unit& u, int wr, int wc, int fr, int fq, const LAS unsigned char* st) const {
;         const int row0 = u.pm * BM + wr * 64 + fr, f0 = u.pn * HALF + wc * 32 + 8 * fq;
;         f32x2 bg[4], bl[4];
;         { const LAS float* sb = (const LAS float*)(st + 512 + fq * 64);
; #pragma unroll
;           for (int p = 0; p < 4; ++p) { bg[p][0] = sb[4 * p]; bg[p][1] = sb[4 * p + 2]; bl[p][0] = sb[4 * p + 1]; bl[p][1] = sb[4 * p + 3]; } }
; #pragma unroll
;         for (int ai = 0; ai < 2; ++ai)
; #pragma unroll
;             for (int mp = 0; mp < 2; ++mp) {
;                 u32x2 w2[2];
; #pragma unroll
;                 for (int mm = 0; mm < 2; ++mm) { const int m = 2 * mp + mm; const float ws = *(const LAS float*)(st + ai * 256 + (m * 16 + fr) * 4) * (1.0f / 32.0f);
;                     const f32x4 g0 = acc[ai][0][m][0], g1 = acc[ai][0][m][1], l0 = acc[ai][1][m][0], l1 = acc[ai][1][m][1];
;                     f32x2 ws2; ws2[0] = ws; ws2[1] = ws;
;                     const f32x2 a01 = swiglu4_2(__builtin_shufflevector(g0, g0, 0, 1) * ws2 + bg[0], __builtin_shufflevector(l0, l0, 0, 1) * ws2 + bl[0]);
;                     const f32x2 a23 = swiglu4_2(__builtin_shufflevector(g0, g0, 2, 3) * ws2 + bg[1], __builtin_shufflevector(l0, l0, 2, 3) * ws2 + bl[1]);
;                     const f32x2 a45 = swiglu4_2(__builtin_shufflevector(g1, g1, 0, 1) * ws2 + bg[2], __builtin_shufflevector(l1, l1, 0, 1) * ws2 + bl[2]);
;                     const f32x2 a67 = swiglu4_2(__builtin_shufflevector(g1, g1, 2, 3) * ws2 + bg[3], __builtin_shufflevector(l1, l1, 2, 3) * ws2 + bl[3]);
;                     w2[mm].x = pk4_fp8n(a01[0], a01[1], a23[0], a23[1]); w2[mm].y = pk4_fp8n(a45[0], a45[1], a67[0], a67[1]); }
.LBB0_1091:
	v_readlane_b32 s32, v254, 23
	s_and_b32 vcc_lo, s71, 7
	s_nop 1
	s_lshl_b32 s32, s32, 13
	s_lshl_b32 vcc_lo, vcc_lo, 16
	s_add_i32 s32, s32, vcc_lo
	v_lshl_add_u32 v255, v224, 7, s32
	global_load_dword v255, v255, s[82:83]
	v_mov_b32_e32 v110, v224
	s_lshl_b32 s1, s34, 7
	v_ashrrev_i32_e32 v168, 4, v110
	v_and_b32_e32 v146, 15, v110
	v_lshl_add_u32 v110, v168, 6, s35
	ds_read_b128 v[130:133], v110 offset:512
	ds_read_b128 v[126:129], v110 offset:528
	ds_read_b128 v[118:121], v110 offset:544
	ds_read_b128 v[110:113], v110 offset:560
	s_or_b32 s1, s1, s58
	s_lshl_b32 s0, s33, 8
	s_waitcnt lgkmcnt(0)
	v_mov_b32_e32 v154, v126
	v_lshl_add_u32 v126, v146, 2, s35
	v_mov_b32_e32 v156, v130
	v_mov_b32_e32 v157, v132
	v_mov_b32_e32 v132, v131
	ds_read2_b32 v[130:131], v126 offset1:16
	v_mov_b32_e32 v150, v110
	v_mov_b32_e32 v151, v112
	v_mov_b32_e32 v112, v111
	v_lshl_add_u32 v110, v168, 3, s1
	s_waitcnt lgkmcnt(0)
	v_mul_f32_e32 v130, 0x3d000000, v130
	v_pk_fma_f32 v[142:143], v[142:143], v[130:131], v[156:157] op_sel_hi:[1,0,1]
	v_and_b32_e32 v111, 1, v168
	v_min_f32_e32 v142, 0x40e00000, v142
	v_min_f32_e32 v143, 0x40e00000, v143
	v_pk_mul_f32 v[168:169], v[142:143], s[84:85] op_sel_hi:[1,0]
	v_mov_b32_e32 v155, v128
	v_exp_f32_e32 v168, v168
	v_exp_f32_e32 v169, v169
	v_pk_fma_f32 v[144:145], v[144:145], v[130:131], v[154:155] op_sel_hi:[1,0,1]
	v_pk_fma_f32 v[138:139], v[138:139], v[130:131], v[132:133] op_sel_hi:[1,0,1]
	v_min_f32_e32 v144, 0x40e00000, v144
	v_pk_add_f32 v[168:169], v[168:169], 1.0 op_sel_hi:[1,0]
	v_min_f32_e32 v145, 0x40e00000, v145
	v_rcp_f32_e32 v168, v168
	v_rcp_f32_e32 v169, v169
	v_pk_mul_f32 v[170:171], v[144:145], s[84:85] op_sel_hi:[1,0]
	v_med3_f32 v138, v138, s69, v167
	v_exp_f32_e32 v170, v170
	v_exp_f32_e32 v171, v171
	v_med3_f32 v139, v139, s69, v167
	v_pk_mul_f32 v[142:143], v[142:143], v[168:169]
	v_pk_fma_f32 v[138:139], v[138:139], 4.0, 4.0 op_sel_hi:[1,0,0]
	v_mov_b32_e32 v128, v127
	v_pk_mul_f32 v[138:139], v[138:139], v[142:143]
	v_pk_add_f32 v[142:143], v[170:171], 1.0 op_sel_hi:[1,0]
	v_mov_b32_e32 v152, v118
	v_rcp_f32_e32 v142, v142
	v_rcp_f32_e32 v143, v143
	v_mov_b32_e32 v153, v120
	v_pk_fma_f32 v[140:141], v[140:141], v[130:131], v[128:129] op_sel_hi:[1,0,1]
	v_pk_fma_f32 v[134:135], v[134:135], v[130:131], v[152:153] op_sel_hi:[1,0,1]
	v_med3_f32 v140, v140, s69, v167
	v_med3_f32 v141, v141, s69, v167
	v_pk_mul_f32 v[142:143], v[144:145], v[142:143]
	v_pk_fma_f32 v[140:141], v[140:141], 4.0, 4.0 op_sel_hi:[1,0,0]
	v_min_f32_e32 v134, 0x40e00000, v134
	v_min_f32_e32 v135, 0x40e00000, v135
	v_pk_mul_f32 v[140:141], v[140:141], v[142:143]
	v_pk_mul_f32 v[142:143], v[134:135], s[84:85] op_sel_hi:[1,0]
	v_pk_fma_f32 v[136:137], v[136:137], v[130:131], v[150:151] op_sel_hi:[1,0,1]
	v_exp_f32_e32 v142, v142
	v_exp_f32_e32 v143, v143
	v_min_f32_e32 v136, 0x40e00000, v136
	v_min_f32_e32 v137, 0x40e00000, v137
	v_pk_mul_f32 v[144:145], v[136:137], s[84:85] op_sel_hi:[1,0]
	v_pk_add_f32 v[142:143], v[142:143], 1.0 op_sel_hi:[1,0]
	v_mov_b32_e32 v120, v119
	v_rcp_f32_e32 v142, v142
	v_rcp_f32_e32 v143, v143
	v_exp_f32_e32 v144, v144
	v_exp_f32_e32 v145, v145
	v_pk_fma_f32 v[122:123], v[122:123], v[130:131], v[120:121] op_sel_hi:[1,0,1]
	v_pk_mul_f32 v[134:135], v[134:135], v[142:143]
	v_med3_f32 v122, v122, s69, v167
	v_med3_f32 v123, v123, s69, v167
	v_pk_fma_f32 v[122:123], v[122:123], 4.0, 4.0 op_sel_hi:[1,0,0]
	v_pk_fma_f32 v[124:125], v[124:125], v[130:131], v[112:113] op_sel_hi:[1,0,1]
	v_pk_mul_f32 v[134:135], v[122:123], v[134:135]
	v_pk_add_f32 v[122:123], v[144:145], 1.0 op_sel_hi:[1,0]
	v_med3_f32 v124, v124, s69, v167
	v_rcp_f32_e32 v122, v122
	v_rcp_f32_e32 v123, v123
	v_med3_f32 v125, v125, s69, v167
	v_pk_fma_f32 v[124:125], v[124:125], 4.0, 4.0 op_sel_hi:[1,0,0]
	s_add_i32 s0, s0, s47
	v_pk_mul_f32 v[136:137], v[136:137], v[122:123]
	v_mov_b32_e32 v123, v147
	v_cvt_pk_fp8_f32 v123, v134, v135
	v_pk_mul_f32 v[124:125], v[124:125], v[136:137]
	v_mov_b32_e32 v122, v147
	v_cvt_pk_fp8_f32 v122, v138, v139
	v_cvt_pk_fp8_f32 v123, v124, v125 op_sel:[0,0,1]
	v_mul_f32_e32 v124, 0x3d000000, v131
	v_pk_fma_f32 v[114:115], v[114:115], v[124:125], v[156:157] op_sel_hi:[1,0,1]
	v_pk_fma_f32 v[116:117], v[116:117], v[124:125], v[154:155] op_sel_hi:[1,0,1]
	v_min_f32_e32 v114, 0x40e00000, v114
	v_min_f32_e32 v115, 0x40e00000, v115
	v_pk_mul_f32 v[130:131], v[114:115], s[84:85] op_sel_hi:[1,0]
	v_min_f32_e32 v116, 0x40e00000, v116
	v_exp_f32_e32 v130, v130
	v_exp_f32_e32 v131, v131
	v_min_f32_e32 v117, 0x40e00000, v117
	v_pk_mul_f32 v[134:135], v[116:117], s[84:85] op_sel_hi:[1,0]
	v_pk_fma_f32 v[106:107], v[106:107], v[124:125], v[132:133] op_sel_hi:[1,0,1]
	v_pk_add_f32 v[130:131], v[130:131], 1.0 op_sel_hi:[1,0]
	v_exp_f32_e32 v134, v134
	v_rcp_f32_e32 v130, v130
	v_rcp_f32_e32 v131, v131
	v_exp_f32_e32 v135, v135
	v_med3_f32 v106, v106, s69, v167
	v_med3_f32 v107, v107, s69, v167
	v_pk_mul_f32 v[114:115], v[114:115], v[130:131]
	v_pk_fma_f32 v[106:107], v[106:107], 4.0, 4.0 op_sel_hi:[1,0,0]
	v_pk_fma_f32 v[108:109], v[108:109], v[124:125], v[128:129] op_sel_hi:[1,0,1]
	v_pk_mul_f32 v[106:107], v[106:107], v[114:115]
	v_pk_add_f32 v[114:115], v[134:135], 1.0 op_sel_hi:[1,0]
	v_med3_f32 v108, v108, s69, v167
	v_rcp_f32_e32 v114, v114
	v_rcp_f32_e32 v115, v115
	v_med3_f32 v109, v109, s69, v167
	v_pk_fma_f32 v[102:103], v[102:103], v[124:125], v[152:153] op_sel_hi:[1,0,1]
	v_pk_fma_f32 v[108:109], v[108:109], 4.0, 4.0 op_sel_hi:[1,0,0]
	v_pk_mul_f32 v[114:115], v[116:117], v[114:115]
	v_min_f32_e32 v102, 0x40e00000, v102
	v_min_f32_e32 v103, 0x40e00000, v103
	v_pk_mul_f32 v[108:109], v[108:109], v[114:115]
; #define LAS __attribute__((address_space(3)))
; DI unsigned pk4_fp8n(float a, float b, float c, float d) { int v = __builtin_amdgcn_cvt_pk_fp8_f32(a, b, 0, false); v = __builtin_amdgcn_cvt_pk_fp8_f32(c, d, v, true); return (unsigned)v; }
; DI f32x2 swiglu4_2(f32x2 hg, f32x2 hl) {
;     f32x2 glu, lin, ex, sg;
;     glu[0] = fminf(hg[0], 7.0f); glu[1] = fminf(hg[1], 7.0f); lin[0] = __builtin_amdgcn_fmed3f(hl[0], -7.0f, 7.0f); lin[1] = __builtin_amdgcn_fmed3f(hl[1], -7.0f, 7.0f);
;     const f32x2 t = glu * (-1.702f * 1.4426950408889634f);
;     ex[0] = __builtin_amdgcn_exp2f(t[0]); ex[1] = __builtin_amdgcn_exp2f(t[1]);
;     const f32x2 den = ex + 1.0f;
;     sg[0] = __builtin_amdgcn_rcpf(den[0]); sg[1] = __builtin_amdgcn_rcpf(den[1]);
;     return (glu * sg) * (lin * 4.0f + 4.0f);
; }
;     DI void operator()(const f32x4 (&acc)[2][2][4][2], const Unit& u, int wr, int wc, int fr, int fq, const LAS unsigned char* st) const {
;     ...
;                 for (int mm = 0; mm < 2; ++mm) { const int m = 2 * mp + mm; const float ws = *(const LAS float*)(st + ai * 256 + (m * 16 + fr) * 4) * (1.0f / 32.0f);
;                     const f32x4 g0 = acc[ai][0][m][0], g1 = acc[ai][0][m][1], l0 = acc[ai][1][m][0], l1 = acc[ai][1][m][1];
;                     f32x2 ws2; ws2[0] = ws; ws2[1] = ws;
;                     const f32x2 a01 = swiglu4_2(__builtin_shufflevector(g0, g0, 0, 1) * ws2 + bg[0], __builtin_shufflevector(l0, l0, 0, 1) * ws2 + bl[0]);
;                     const f32x2 a23 = swiglu4_2(__builtin_shufflevector(g0, g0, 2, 3) * ws2 + bg[1], __builtin_shufflevector(l0, l0, 2, 3) * ws2 + bl[1]);
;                     const f32x2 a45 = swiglu4_2(__builtin_shufflevector(g1, g1, 0, 1) * ws2 + bg[2], __builtin_shufflevector(l1, l1, 0, 1) * ws2 + bl[2]);
;                     const f32x2 a67 = swiglu4_2(__builtin_shufflevector(g1, g1, 2, 3) * ws2 + bg[3], __builtin_shufflevector(l1, l1, 2, 3) * ws2 + bl[3]);
;                     w2[mm].x = pk4_fp8n(a01[0], a01[1], a23[0], a23[1]); w2[mm].y = pk4_fp8n(a45[0], a45[1], a67[0], a67[1]); }
;                 const u32x4 w = pair16(w2[0], w2[1]);
;                 *(u32x4*)(ACT + (size_t)(row0 + ai * HALF + (2 * mp + (fq & 1)) * 16) * FF + (f0 - 8 * (fq & 1))) = w; }
	v_pk_mul_f32 v[114:115], v[102:103], s[84:85] op_sel_hi:[1,0]
	v_pk_fma_f32 v[104:105], v[104:105], v[124:125], v[150:151] op_sel_hi:[1,0,1]
	v_exp_f32_e32 v114, v114
	v_exp_f32_e32 v115, v115
	v_min_f32_e32 v104, 0x40e00000, v104
	v_min_f32_e32 v105, 0x40e00000, v105
	v_pk_mul_f32 v[116:117], v[104:105], s[84:85] op_sel_hi:[1,0]
	v_pk_add_f32 v[114:115], v[114:115], 1.0 op_sel_hi:[1,0]
	v_exp_f32_e32 v116, v116
	v_rcp_f32_e32 v114, v114
	v_rcp_f32_e32 v115, v115
	v_exp_f32_e32 v117, v117
	v_pk_fma_f32 v[98:99], v[98:99], v[124:125], v[120:121] op_sel_hi:[1,0,1]
	v_pk_fma_f32 v[100:101], v[100:101], v[124:125], v[112:113] op_sel_hi:[1,0,1]
	v_med3_f32 v98, v98, s69, v167
	v_med3_f32 v99, v99, s69, v167
	v_pk_mul_f32 v[102:103], v[102:103], v[114:115]
	v_pk_fma_f32 v[98:99], v[98:99], 4.0, 4.0 op_sel_hi:[1,0,0]
	v_mov_b32_e32 v125, v147
	v_pk_mul_f32 v[98:99], v[98:99], v[102:103]
	v_pk_add_f32 v[102:103], v[116:117], 1.0 op_sel_hi:[1,0]
	v_cvt_pk_fp8_f32 v125, v98, v99
	v_rcp_f32_e32 v102, v102
	v_rcp_f32_e32 v103, v103
	v_med3_f32 v100, v100, s69, v167
	v_med3_f32 v101, v101, s69, v167
	v_mov_b32_e32 v124, v147
	v_pk_mul_f32 v[102:103], v[104:105], v[102:103]
	v_pk_fma_f32 v[98:99], v[100:101], 4.0, 4.0 op_sel_hi:[1,0,0]
	v_cvt_pk_fp8_f32 v124, v106, v107
	v_pk_mul_f32 v[98:99], v[98:99], v[102:103]
	v_lshlrev_b32_e32 v118, 4, v111
	v_cvt_pk_fp8_f32 v125, v98, v99 op_sel:[0,0,1]
	ds_read2_b32 v[98:99], v126 offset0:32 offset1:48
	v_or3_b32 v118, v118, s0, v146
	v_cvt_pk_fp8_f32 v122, v140, v141 op_sel:[0,0,1]
	v_cvt_pk_fp8_f32 v124, v108, v109 op_sel:[0,0,1]
	v_lshlrev_b32_e32 v111, 3, v111
	v_ashrrev_i32_e32 v119, 31, v118
	v_sub_u32_e32 v110, v110, v111
	v_lshlrev_b64 v[100:101], 11, v[118:119]
	s_waitcnt lgkmcnt(0)
	v_mul_f32_e32 v98, 0x3d000000, v98
	v_ashrrev_i32_e32 v111, 31, v110
	v_lshl_add_u64 v[100:101], s[86:87], 0, v[100:101]
	v_pk_fma_f32 v[94:95], v[94:95], v[98:99], v[156:157] op_sel_hi:[1,0,1]
	v_permlane16_swap_b32_e32 v122, v124
	v_permlane16_swap_b32_e32 v123, v125
	v_lshl_add_u64 v[100:101], v[100:101], 0, v[110:111]
	v_min_f32_e32 v94, 0x40e00000, v94
	v_min_f32_e32 v95, 0x40e00000, v95
	global_store_dwordx4 v[100:101], v[122:125], off
	v_pk_mul_f32 v[100:101], v[94:95], s[84:85] op_sel_hi:[1,0]
	v_pk_fma_f32 v[96:97], v[96:97], v[98:99], v[154:155] op_sel_hi:[1,0,1]
	v_exp_f32_e32 v100, v100
	v_exp_f32_e32 v101, v101
	v_min_f32_e32 v96, 0x40e00000, v96
	v_min_f32_e32 v97, 0x40e00000, v97
	v_pk_mul_f32 v[102:103], v[96:97], s[84:85] op_sel_hi:[1,0]
	v_pk_add_f32 v[100:101], v[100:101], 1.0 op_sel_hi:[1,0]
	v_exp_f32_e32 v102, v102
	v_rcp_f32_e32 v100, v100
	v_rcp_f32_e32 v101, v101
	v_exp_f32_e32 v103, v103
	v_pk_fma_f32 v[90:91], v[90:91], v[98:99], v[132:133] op_sel_hi:[1,0,1]
	v_pk_fma_f32 v[92:93], v[92:93], v[98:99], v[128:129] op_sel_hi:[1,0,1]
	v_med3_f32 v90, v90, s69, v167
	v_med3_f32 v91, v91, s69, v167
	v_pk_mul_f32 v[94:95], v[94:95], v[100:101]
	v_pk_fma_f32 v[90:91], v[90:91], 4.0, 4.0 op_sel_hi:[1,0,0]
	v_med3_f32 v92, v92, s69, v167
	v_pk_mul_f32 v[90:91], v[90:91], v[94:95]
	v_pk_add_f32 v[94:95], v[102:103], 1.0 op_sel_hi:[1,0]
	v_med3_f32 v93, v93, s69, v167
	v_rcp_f32_e32 v94, v94
	v_rcp_f32_e32 v95, v95
	v_pk_fma_f32 v[86:87], v[86:87], v[98:99], v[152:153] op_sel_hi:[1,0,1]
	v_pk_fma_f32 v[92:93], v[92:93], 4.0, 4.0 op_sel_hi:[1,0,0]
	v_min_f32_e32 v86, 0x40e00000, v86
	v_pk_mul_f32 v[94:95], v[96:97], v[94:95]
	v_min_f32_e32 v87, 0x40e00000, v87
	v_pk_mul_f32 v[92:93], v[92:93], v[94:95]
	v_pk_mul_f32 v[94:95], v[86:87], s[84:85] op_sel_hi:[1,0]
	v_pk_fma_f32 v[88:89], v[88:89], v[98:99], v[150:151] op_sel_hi:[1,0,1]
	v_exp_f32_e32 v94, v94
	v_exp_f32_e32 v95, v95
	v_min_f32_e32 v88, 0x40e00000, v88
	v_min_f32_e32 v89, 0x40e00000, v89
	v_pk_mul_f32 v[96:97], v[88:89], s[84:85] op_sel_hi:[1,0]
	v_pk_add_f32 v[94:95], v[94:95], 1.0 op_sel_hi:[1,0]
	v_exp_f32_e32 v96, v96
	v_rcp_f32_e32 v94, v94
	v_rcp_f32_e32 v95, v95
	v_exp_f32_e32 v97, v97
	v_pk_fma_f32 v[82:83], v[82:83], v[98:99], v[120:121] op_sel_hi:[1,0,1]
	v_pk_fma_f32 v[84:85], v[84:85], v[98:99], v[112:113] op_sel_hi:[1,0,1]
	v_med3_f32 v82, v82, s69, v167
	v_med3_f32 v83, v83, s69, v167
	v_pk_mul_f32 v[86:87], v[86:87], v[94:95]
	v_pk_fma_f32 v[82:83], v[82:83], 4.0, 4.0 op_sel_hi:[1,0,0]
	v_med3_f32 v84, v84, s69, v167
	v_pk_mul_f32 v[86:87], v[82:83], v[86:87]
	v_pk_add_f32 v[82:83], v[96:97], 1.0 op_sel_hi:[1,0]
	v_med3_f32 v85, v85, s69, v167
	v_rcp_f32_e32 v82, v82
	v_rcp_f32_e32 v83, v83
	v_pk_fma_f32 v[84:85], v[84:85], 4.0, 4.0 op_sel_hi:[1,0,0]
	s_and_b64 vcc, exec, s[2:3]
	s_mov_b64 s[0:1], -1
	v_pk_mul_f32 v[88:89], v[88:89], v[82:83]
	v_mov_b32_e32 v83, v147
	v_cvt_pk_fp8_f32 v83, v86, v87
	v_pk_mul_f32 v[84:85], v[84:85], v[88:89]
	v_mov_b32_e32 v82, v147
	v_cvt_pk_fp8_f32 v82, v90, v91
	v_cvt_pk_fp8_f32 v83, v84, v85 op_sel:[0,0,1]
	v_mul_f32_e32 v84, 0x3d000000, v99
	v_pk_fma_f32 v[78:79], v[78:79], v[84:85], v[156:157] op_sel_hi:[1,0,1]
	v_pk_fma_f32 v[80:81], v[80:81], v[84:85], v[154:155] op_sel_hi:[1,0,1]
	v_min_f32_e32 v78, 0x40e00000, v78
	v_min_f32_e32 v79, 0x40e00000, v79
	v_pk_mul_f32 v[86:87], v[78:79], s[84:85] op_sel_hi:[1,0]
	v_min_f32_e32 v80, 0x40e00000, v80
	v_exp_f32_e32 v86, v86
	v_exp_f32_e32 v87, v87
	v_min_f32_e32 v81, 0x40e00000, v81
	v_pk_mul_f32 v[88:89], v[80:81], s[84:85] op_sel_hi:[1,0]
	v_pk_fma_f32 v[74:75], v[74:75], v[84:85], v[132:133] op_sel_hi:[1,0,1]
	v_pk_add_f32 v[86:87], v[86:87], 1.0 op_sel_hi:[1,0]
	v_exp_f32_e32 v88, v88
	v_rcp_f32_e32 v86, v86
	v_rcp_f32_e32 v87, v87
	v_exp_f32_e32 v89, v89
	v_med3_f32 v74, v74, s69, v167
	v_med3_f32 v75, v75, s69, v167
; #define LAS __attribute__((address_space(3)))
; DI unsigned pk4_fp8n(float a, float b, float c, float d) { int v = __builtin_amdgcn_cvt_pk_fp8_f32(a, b, 0, false); v = __builtin_amdgcn_cvt_pk_fp8_f32(c, d, v, true); return (unsigned)v; }
; DI f32x2 swiglu4_2(f32x2 hg, f32x2 hl) {
;     f32x2 glu, lin, ex, sg;
;     glu[0] = fminf(hg[0], 7.0f); glu[1] = fminf(hg[1], 7.0f); lin[0] = __builtin_amdgcn_fmed3f(hl[0], -7.0f, 7.0f); lin[1] = __builtin_amdgcn_fmed3f(hl[1], -7.0f, 7.0f);
;     const f32x2 t = glu * (-1.702f * 1.4426950408889634f);
;     ex[0] = __builtin_amdgcn_exp2f(t[0]); ex[1] = __builtin_amdgcn_exp2f(t[1]);
;     const f32x2 den = ex + 1.0f;
;     sg[0] = __builtin_amdgcn_rcpf(den[0]); sg[1] = __builtin_amdgcn_rcpf(den[1]);
;     return (glu * sg) * (lin * 4.0f + 4.0f);
; }
;     DI void operator()(const f32x4 (&acc)[2][2][4][2], const Unit& u, int wr, int wc, int fr, int fq, const LAS unsigned char* st) const {
;     ...
;                 for (int mm = 0; mm < 2; ++mm) { const int m = 2 * mp + mm; const float ws = *(const LAS float*)(st + ai * 256 + (m * 16 + fr) * 4) * (1.0f / 32.0f);
;                     const f32x4 g0 = acc[ai][0][m][0], g1 = acc[ai][0][m][1], l0 = acc[ai][1][m][0], l1 = acc[ai][1][m][1];
;                     f32x2 ws2; ws2[0] = ws; ws2[1] = ws;
;                     const f32x2 a01 = swiglu4_2(__builtin_shufflevector(g0, g0, 0, 1) * ws2 + bg[0], __builtin_shufflevector(l0, l0, 0, 1) * ws2 + bl[0]);
;                     const f32x2 a23 = swiglu4_2(__builtin_shufflevector(g0, g0, 2, 3) * ws2 + bg[1], __builtin_shufflevector(l0, l0, 2, 3) * ws2 + bl[1]);
;                     const f32x2 a45 = swiglu4_2(__builtin_shufflevector(g1, g1, 0, 1) * ws2 + bg[2], __builtin_shufflevector(l1, l1, 0, 1) * ws2 + bl[2]);
;                     const f32x2 a67 = swiglu4_2(__builtin_shufflevector(g1, g1, 2, 3) * ws2 + bg[3], __builtin_shufflevector(l1, l1, 2, 3) * ws2 + bl[3]);
;                     w2[mm].x = pk4_fp8n(a01[0], a01[1], a23[0], a23[1]); w2[mm].y = pk4_fp8n(a45[0], a45[1], a67[0], a67[1]); }
;                 const u32x4 w = pair16(w2[0], w2[1]);
;                 *(u32x4*)(ACT + (size_t)(row0 + ai * HALF + (2 * mp + (fq & 1)) * 16) * FF + (f0 - 8 * (fq & 1))) = w; }
	v_pk_mul_f32 v[78:79], v[78:79], v[86:87]
	v_pk_fma_f32 v[74:75], v[74:75], 4.0, 4.0 op_sel_hi:[1,0,0]
	v_pk_fma_f32 v[76:77], v[76:77], v[84:85], v[128:129] op_sel_hi:[1,0,1]
	v_pk_mul_f32 v[74:75], v[74:75], v[78:79]
	v_pk_add_f32 v[78:79], v[88:89], 1.0 op_sel_hi:[1,0]
	v_med3_f32 v76, v76, s69, v167
	v_rcp_f32_e32 v78, v78
	v_rcp_f32_e32 v79, v79
	v_med3_f32 v77, v77, s69, v167
	v_pk_fma_f32 v[70:71], v[70:71], v[84:85], v[152:153] op_sel_hi:[1,0,1]
	v_pk_fma_f32 v[76:77], v[76:77], 4.0, 4.0 op_sel_hi:[1,0,0]
	v_pk_mul_f32 v[78:79], v[80:81], v[78:79]
	v_min_f32_e32 v70, 0x40e00000, v70
	v_min_f32_e32 v71, 0x40e00000, v71
	v_pk_mul_f32 v[76:77], v[76:77], v[78:79]
	v_pk_mul_f32 v[78:79], v[70:71], s[84:85] op_sel_hi:[1,0]
	v_pk_fma_f32 v[72:73], v[72:73], v[84:85], v[150:151] op_sel_hi:[1,0,1]
	v_exp_f32_e32 v78, v78
	v_exp_f32_e32 v79, v79
	v_pk_fma_f32 v[66:67], v[66:67], v[84:85], v[120:121] op_sel_hi:[1,0,1]
	v_min_f32_e32 v72, 0x40e00000, v72
	v_min_f32_e32 v73, 0x40e00000, v73
	v_pk_add_f32 v[78:79], v[78:79], 1.0 op_sel_hi:[1,0]
	v_med3_f32 v66, v66, s69, v167
	v_rcp_f32_e32 v78, v78
	v_rcp_f32_e32 v79, v79
	v_med3_f32 v67, v67, s69, v167
	v_pk_mul_f32 v[80:81], v[72:73], s[84:85] op_sel_hi:[1,0]
	v_pk_fma_f32 v[66:67], v[66:67], 4.0, 4.0 op_sel_hi:[1,0,0]
	v_exp_f32_e32 v80, v80
	v_exp_f32_e32 v81, v81
	v_pk_mul_f32 v[70:71], v[70:71], v[78:79]
	v_pk_fma_f32 v[68:69], v[68:69], v[84:85], v[112:113] op_sel_hi:[1,0,1]
	v_pk_mul_f32 v[66:67], v[66:67], v[70:71]
	v_med3_f32 v68, v68, s69, v167
	v_med3_f32 v69, v69, s69, v167
	v_mov_b32_e32 v85, v147
	v_cvt_pk_fp8_f32 v85, v66, v67
	v_pk_fma_f32 v[66:67], v[68:69], 4.0, 4.0 op_sel_hi:[1,0,0]
	ds_read2_b32 v[68:69], v126 offset0:64 offset1:80
	v_pk_add_f32 v[70:71], v[80:81], 1.0 op_sel_hi:[1,0]
	v_mov_b32_e32 v84, v147
	v_rcp_f32_e32 v70, v70
	v_rcp_f32_e32 v71, v71
	s_waitcnt lgkmcnt(0)
	v_mul_f32_e32 v68, 0x3d000000, v68
	v_pk_fma_f32 v[62:63], v[62:63], v[68:69], v[156:157] op_sel_hi:[1,0,1]
	v_pk_fma_f32 v[64:65], v[64:65], v[68:69], v[154:155] op_sel_hi:[1,0,1]
	v_pk_mul_f32 v[70:71], v[72:73], v[70:71]
	v_min_f32_e32 v62, 0x40e00000, v62
	v_min_f32_e32 v63, 0x40e00000, v63
	v_pk_mul_f32 v[66:67], v[66:67], v[70:71]
	v_pk_mul_f32 v[70:71], v[62:63], s[84:85] op_sel_hi:[1,0]
	v_min_f32_e32 v64, 0x40e00000, v64
	v_exp_f32_e32 v70, v70
	v_exp_f32_e32 v71, v71
	v_min_f32_e32 v65, 0x40e00000, v65
	v_pk_mul_f32 v[72:73], v[64:65], s[84:85] op_sel_hi:[1,0]
	v_pk_fma_f32 v[58:59], v[58:59], v[68:69], v[132:133] op_sel_hi:[1,0,1]
	v_pk_add_f32 v[70:71], v[70:71], 1.0 op_sel_hi:[1,0]
	v_exp_f32_e32 v72, v72
	v_rcp_f32_e32 v70, v70
	v_rcp_f32_e32 v71, v71
	v_exp_f32_e32 v73, v73
	v_med3_f32 v58, v58, s69, v167
	v_med3_f32 v59, v59, s69, v167
	v_pk_mul_f32 v[62:63], v[62:63], v[70:71]
	v_pk_fma_f32 v[58:59], v[58:59], 4.0, 4.0 op_sel_hi:[1,0,0]
	v_pk_fma_f32 v[60:61], v[60:61], v[68:69], v[128:129] op_sel_hi:[1,0,1]
	v_pk_mul_f32 v[58:59], v[58:59], v[62:63]
	v_pk_add_f32 v[62:63], v[72:73], 1.0 op_sel_hi:[1,0]
	v_med3_f32 v60, v60, s69, v167
	v_rcp_f32_e32 v62, v62
	v_rcp_f32_e32 v63, v63
	v_med3_f32 v61, v61, s69, v167
	v_pk_fma_f32 v[54:55], v[54:55], v[68:69], v[152:153] op_sel_hi:[1,0,1]
	v_pk_fma_f32 v[60:61], v[60:61], 4.0, 4.0 op_sel_hi:[1,0,0]
	v_pk_mul_f32 v[62:63], v[64:65], v[62:63]
	v_min_f32_e32 v54, 0x40e00000, v54
	v_min_f32_e32 v55, 0x40e00000, v55
	v_pk_mul_f32 v[60:61], v[60:61], v[62:63]
	v_pk_mul_f32 v[62:63], v[54:55], s[84:85] op_sel_hi:[1,0]
	v_pk_fma_f32 v[56:57], v[56:57], v[68:69], v[150:151] op_sel_hi:[1,0,1]
	v_exp_f32_e32 v62, v62
	v_exp_f32_e32 v63, v63
	v_min_f32_e32 v56, 0x40e00000, v56
	v_min_f32_e32 v57, 0x40e00000, v57
	v_pk_mul_f32 v[64:65], v[56:57], s[84:85] op_sel_hi:[1,0]
	v_pk_add_f32 v[62:63], v[62:63], 1.0 op_sel_hi:[1,0]
	v_exp_f32_e32 v64, v64
	v_rcp_f32_e32 v62, v62
	v_rcp_f32_e32 v63, v63
	v_exp_f32_e32 v65, v65
	v_pk_fma_f32 v[50:51], v[50:51], v[68:69], v[120:121] op_sel_hi:[1,0,1]
	v_pk_fma_f32 v[52:53], v[52:53], v[68:69], v[112:113] op_sel_hi:[1,0,1]
	v_med3_f32 v50, v50, s69, v167
	v_med3_f32 v51, v51, s69, v167
	v_pk_mul_f32 v[54:55], v[54:55], v[62:63]
	v_pk_fma_f32 v[50:51], v[50:51], 4.0, 4.0 op_sel_hi:[1,0,0]
	v_med3_f32 v52, v52, s69, v167
	v_pk_mul_f32 v[54:55], v[50:51], v[54:55]
	v_pk_add_f32 v[50:51], v[64:65], 1.0 op_sel_hi:[1,0]
	v_med3_f32 v53, v53, s69, v167
	v_rcp_f32_e32 v50, v50
	v_rcp_f32_e32 v51, v51
	v_pk_fma_f32 v[52:53], v[52:53], 4.0, 4.0 op_sel_hi:[1,0,0]
	v_cvt_pk_fp8_f32 v84, v74, v75
	v_cvt_pk_fp8_f32 v82, v92, v93 op_sel:[0,0,1]
	v_pk_mul_f32 v[56:57], v[56:57], v[50:51]
	v_mov_b32_e32 v51, v147
	v_cvt_pk_fp8_f32 v51, v54, v55
	v_pk_mul_f32 v[52:53], v[52:53], v[56:57]
	v_cvt_pk_fp8_f32 v84, v76, v77 op_sel:[0,0,1]
	v_cvt_pk_fp8_f32 v85, v66, v67 op_sel:[0,0,1]
	v_cvt_pk_fp8_f32 v51, v52, v53 op_sel:[0,0,1]
	v_mul_f32_e32 v52, 0x3d000000, v69
	v_pk_fma_f32 v[46:47], v[46:47], v[52:53], v[156:157] op_sel_hi:[1,0,1]
	v_pk_fma_f32 v[48:49], v[48:49], v[52:53], v[154:155] op_sel_hi:[1,0,1]
	v_min_f32_e32 v46, 0x40e00000, v46
	v_min_f32_e32 v47, 0x40e00000, v47
	v_pk_mul_f32 v[54:55], v[46:47], s[84:85] op_sel_hi:[1,0]
	v_min_f32_e32 v48, 0x40e00000, v48
	v_exp_f32_e32 v54, v54
	v_exp_f32_e32 v55, v55
	v_min_f32_e32 v49, 0x40e00000, v49
	v_pk_mul_f32 v[56:57], v[48:49], s[84:85] op_sel_hi:[1,0]
	v_pk_fma_f32 v[42:43], v[42:43], v[52:53], v[132:133] op_sel_hi:[1,0,1]
	v_pk_add_f32 v[54:55], v[54:55], 1.0 op_sel_hi:[1,0]
	v_exp_f32_e32 v56, v56
	v_rcp_f32_e32 v54, v54
	v_rcp_f32_e32 v55, v55
	v_exp_f32_e32 v57, v57
	v_med3_f32 v42, v42, s69, v167
	v_med3_f32 v43, v43, s69, v167
	v_pk_mul_f32 v[46:47], v[46:47], v[54:55]
; #define LAS __attribute__((address_space(3)))
; DI unsigned pk4_fp8n(float a, float b, float c, float d) { int v = __builtin_amdgcn_cvt_pk_fp8_f32(a, b, 0, false); v = __builtin_amdgcn_cvt_pk_fp8_f32(c, d, v, true); return (unsigned)v; }
;     DI void operator()(const f32x4 (&acc)[2][2][4][2], const Unit& u, int wr, int wc, int fr, int fq, const LAS unsigned char* st) const {
;     ...
;                 for (int mm = 0; mm < 2; ++mm) { const int m = 2 * mp + mm; const float ws = *(const LAS float*)(st + ai * 256 + (m * 16 + fr) * 4) * (1.0f / 32.0f);
;                     const f32x4 g0 = acc[ai][0][m][0], g1 = acc[ai][0][m][1], l0 = acc[ai][1][m][0], l1 = acc[ai][1][m][1];
;                     f32x2 ws2; ws2[0] = ws; ws2[1] = ws;
;                     const f32x2 a01 = swiglu4_2(__builtin_shufflevector(g0, g0, 0, 1) * ws2 + bg[0], __builtin_shufflevector(l0, l0, 0, 1) * ws2 + bl[0]);
;                     const f32x2 a23 = swiglu4_2(__builtin_shufflevector(g0, g0, 2, 3) * ws2 + bg[1], __builtin_shufflevector(l0, l0, 2, 3) * ws2 + bl[1]);
;                     const f32x2 a45 = swiglu4_2(__builtin_shufflevector(g1, g1, 0, 1) * ws2 + bg[2], __builtin_shufflevector(l1, l1, 0, 1) * ws2 + bl[2]);
;                     const f32x2 a67 = swiglu4_2(__builtin_shufflevector(g1, g1, 2, 3) * ws2 + bg[3], __builtin_shufflevector(l1, l1, 2, 3) * ws2 + bl[3]);
;                     w2[mm].x = pk4_fp8n(a01[0], a01[1], a23[0], a23[1]); w2[mm].y = pk4_fp8n(a45[0], a45[1], a67[0], a67[1]); }
;                 const u32x4 w = pair16(w2[0], w2[1]);
;                 *(u32x4*)(ACT + (size_t)(row0 + ai * HALF + (2 * mp + (fq & 1)) * 16) * FF + (f0 - 8 * (fq & 1))) = w; }
	v_pk_fma_f32 v[42:43], v[42:43], 4.0, 4.0 op_sel_hi:[1,0,0]
	v_pk_fma_f32 v[44:45], v[44:45], v[52:53], v[128:129] op_sel_hi:[1,0,1]
	v_pk_mul_f32 v[42:43], v[42:43], v[46:47]
	v_pk_add_f32 v[46:47], v[56:57], 1.0 op_sel_hi:[1,0]
	v_med3_f32 v44, v44, s69, v167
	v_rcp_f32_e32 v46, v46
	v_rcp_f32_e32 v47, v47
	v_med3_f32 v45, v45, s69, v167
	v_pk_fma_f32 v[38:39], v[38:39], v[52:53], v[152:153] op_sel_hi:[1,0,1]
	v_pk_fma_f32 v[44:45], v[44:45], 4.0, 4.0 op_sel_hi:[1,0,0]
	v_pk_mul_f32 v[46:47], v[48:49], v[46:47]
	v_min_f32_e32 v38, 0x40e00000, v38
	v_min_f32_e32 v39, 0x40e00000, v39
	v_pk_mul_f32 v[44:45], v[44:45], v[46:47]
	v_pk_mul_f32 v[46:47], v[38:39], s[84:85] op_sel_hi:[1,0]
	v_pk_fma_f32 v[40:41], v[40:41], v[52:53], v[150:151] op_sel_hi:[1,0,1]
	v_exp_f32_e32 v46, v46
	v_exp_f32_e32 v47, v47
	v_min_f32_e32 v40, 0x40e00000, v40
	v_min_f32_e32 v41, 0x40e00000, v41
	v_pk_mul_f32 v[48:49], v[40:41], s[84:85] op_sel_hi:[1,0]
	v_pk_add_f32 v[46:47], v[46:47], 1.0 op_sel_hi:[1,0]
	v_exp_f32_e32 v48, v48
	v_rcp_f32_e32 v46, v46
	v_rcp_f32_e32 v47, v47
	v_exp_f32_e32 v49, v49
	v_pk_fma_f32 v[34:35], v[34:35], v[52:53], v[120:121] op_sel_hi:[1,0,1]
	v_pk_fma_f32 v[36:37], v[36:37], v[52:53], v[112:113] op_sel_hi:[1,0,1]
	v_med3_f32 v34, v34, s69, v167
	v_med3_f32 v35, v35, s69, v167
	v_pk_mul_f32 v[38:39], v[38:39], v[46:47]
	v_pk_fma_f32 v[34:35], v[34:35], 4.0, 4.0 op_sel_hi:[1,0,0]
	v_mov_b32_e32 v53, v147
	v_pk_mul_f32 v[34:35], v[34:35], v[38:39]
	v_pk_add_f32 v[38:39], v[48:49], 1.0 op_sel_hi:[1,0]
	v_cvt_pk_fp8_f32 v53, v34, v35
	v_rcp_f32_e32 v38, v38
	v_rcp_f32_e32 v39, v39
	v_med3_f32 v36, v36, s69, v167
	v_med3_f32 v37, v37, s69, v167
	v_or_b32_e32 v66, 32, v118
	v_mov_b32_e32 v50, v147
	v_pk_mul_f32 v[38:39], v[40:41], v[38:39]
	v_mov_b32_e32 v52, v147
	v_pk_fma_f32 v[34:35], v[36:37], 4.0, 4.0 op_sel_hi:[1,0,0]
	v_ashrrev_i32_e32 v67, 31, v66
	v_cvt_pk_fp8_f32 v50, v58, v59
	v_cvt_pk_fp8_f32 v52, v42, v43
	v_pk_mul_f32 v[34:35], v[34:35], v[38:39]
	v_lshlrev_b64 v[66:67], 11, v[66:67]
	v_cvt_pk_fp8_f32 v53, v34, v35 op_sel:[0,0,1]
	ds_read2_b32 v[34:35], v126 offset0:96 offset1:112
	v_lshl_add_u64 v[66:67], s[86:87], 0, v[66:67]
	v_permlane16_swap_b32_e32 v82, v84
	v_permlane16_swap_b32_e32 v83, v85
	v_lshl_add_u64 v[66:67], v[66:67], 0, v[110:111]
	global_store_dwordx4 v[66:67], v[82:85], off
	v_add_u32_e32 v66, 0x80, v118
	v_cvt_pk_fp8_f32 v50, v60, v61 op_sel:[0,0,1]
	v_cvt_pk_fp8_f32 v52, v44, v45 op_sel:[0,0,1]
	v_ashrrev_i32_e32 v67, 31, v66
	v_lshlrev_b64 v[36:37], 11, v[66:67]
	s_waitcnt lgkmcnt(0)
	v_mul_f32_e32 v34, 0x3d000000, v34
	v_lshl_add_u64 v[36:37], s[86:87], 0, v[36:37]
	v_pk_fma_f32 v[30:31], v[30:31], v[34:35], v[156:157] op_sel_hi:[1,0,1]
	v_permlane16_swap_b32_e32 v50, v52
	v_permlane16_swap_b32_e32 v51, v53
	v_lshl_add_u64 v[36:37], v[36:37], 0, v[110:111]
	v_min_f32_e32 v30, 0x40e00000, v30
	v_min_f32_e32 v31, 0x40e00000, v31
	global_store_dwordx4 v[36:37], v[50:53], off
	v_pk_mul_f32 v[36:37], v[30:31], s[84:85] op_sel_hi:[1,0]
	v_pk_fma_f32 v[32:33], v[32:33], v[34:35], v[154:155] op_sel_hi:[1,0,1]
	v_exp_f32_e32 v36, v36
	v_exp_f32_e32 v37, v37
	v_min_f32_e32 v32, 0x40e00000, v32
	v_min_f32_e32 v33, 0x40e00000, v33
	v_pk_mul_f32 v[38:39], v[32:33], s[84:85] op_sel_hi:[1,0]
	v_pk_add_f32 v[36:37], v[36:37], 1.0 op_sel_hi:[1,0]
	v_exp_f32_e32 v38, v38
	v_rcp_f32_e32 v36, v36
	v_rcp_f32_e32 v37, v37
	v_exp_f32_e32 v39, v39
	v_pk_fma_f32 v[26:27], v[26:27], v[34:35], v[132:133] op_sel_hi:[1,0,1]
	v_pk_fma_f32 v[28:29], v[28:29], v[34:35], v[128:129] op_sel_hi:[1,0,1]
	v_med3_f32 v26, v26, s69, v167
	v_med3_f32 v27, v27, s69, v167
	v_pk_mul_f32 v[30:31], v[30:31], v[36:37]
	v_pk_fma_f32 v[26:27], v[26:27], 4.0, 4.0 op_sel_hi:[1,0,0]
	v_med3_f32 v28, v28, s69, v167
	v_pk_mul_f32 v[26:27], v[26:27], v[30:31]
	v_pk_add_f32 v[30:31], v[38:39], 1.0 op_sel_hi:[1,0]
	v_med3_f32 v29, v29, s69, v167
	v_rcp_f32_e32 v30, v30
	v_rcp_f32_e32 v31, v31
	v_pk_fma_f32 v[22:23], v[22:23], v[34:35], v[152:153] op_sel_hi:[1,0,1]
	v_pk_fma_f32 v[28:29], v[28:29], 4.0, 4.0 op_sel_hi:[1,0,0]
	v_min_f32_e32 v22, 0x40e00000, v22
	v_pk_mul_f32 v[30:31], v[32:33], v[30:31]
	v_min_f32_e32 v23, 0x40e00000, v23
	v_pk_mul_f32 v[28:29], v[28:29], v[30:31]
	v_pk_mul_f32 v[30:31], v[22:23], s[84:85] op_sel_hi:[1,0]
	v_pk_fma_f32 v[24:25], v[24:25], v[34:35], v[150:151] op_sel_hi:[1,0,1]
	v_exp_f32_e32 v30, v30
	v_exp_f32_e32 v31, v31
	v_min_f32_e32 v24, 0x40e00000, v24
	v_min_f32_e32 v25, 0x40e00000, v25
	v_pk_mul_f32 v[32:33], v[24:25], s[84:85] op_sel_hi:[1,0]
	v_pk_add_f32 v[30:31], v[30:31], 1.0 op_sel_hi:[1,0]
	v_exp_f32_e32 v32, v32
	v_rcp_f32_e32 v30, v30
	v_rcp_f32_e32 v31, v31
	v_exp_f32_e32 v33, v33
	v_pk_fma_f32 v[18:19], v[18:19], v[34:35], v[120:121] op_sel_hi:[1,0,1]
	v_pk_fma_f32 v[20:21], v[20:21], v[34:35], v[112:113] op_sel_hi:[1,0,1]
	v_med3_f32 v18, v18, s69, v167
	v_med3_f32 v19, v19, s69, v167
	v_pk_mul_f32 v[22:23], v[22:23], v[30:31]
; #define LAS __attribute__((address_space(3)))
; DI unsigned pk4_fp8n(float a, float b, float c, float d) { int v = __builtin_amdgcn_cvt_pk_fp8_f32(a, b, 0, false); v = __builtin_amdgcn_cvt_pk_fp8_f32(c, d, v, true); return (unsigned)v; }
; #define PG8_DMA4(gp, lp) __builtin_amdgcn_global_load_lds((const unsigned*)(gp), (LAS unsigned*)(lp), 4, 0, 0)
;     DI void prefetch(const Unit& u, int wr, int wc, int lane, LAS unsigned char* st) const {
;         const float* rp = rows + u.pm * BM + wr * 64 + lane;
;         PG8_DMA4(rp, st); PG8_DMA4(rp + HALF, st + 256);
;         PG8_DMA4(b_up + (size_t)u.e * UPW + 2 * (u.pn * HALF + wc * 32) + lane, st + 512);
;     }
;     DI void operator()(const f32x4 (&acc)[2][2][4][2], const Unit& u, int wr, int wc, int fr, int fq, const LAS unsigned char* st) const {
;     ...
;                 for (int mm = 0; mm < 2; ++mm) { const int m = 2 * mp + mm; const float ws = *(const LAS float*)(st + ai * 256 + (m * 16 + fr) * 4) * (1.0f / 32.0f);
;                     const f32x4 g0 = acc[ai][0][m][0], g1 = acc[ai][0][m][1], l0 = acc[ai][1][m][0], l1 = acc[ai][1][m][1];
;                     f32x2 ws2; ws2[0] = ws; ws2[1] = ws;
;                     const f32x2 a01 = swiglu4_2(__builtin_shufflevector(g0, g0, 0, 1) * ws2 + bg[0], __builtin_shufflevector(l0, l0, 0, 1) * ws2 + bl[0]);
;                     const f32x2 a23 = swiglu4_2(__builtin_shufflevector(g0, g0, 2, 3) * ws2 + bg[1], __builtin_shufflevector(l0, l0, 2, 3) * ws2 + bl[1]);
;                     const f32x2 a45 = swiglu4_2(__builtin_shufflevector(g1, g1, 0, 1) * ws2 + bg[2], __builtin_shufflevector(l1, l1, 0, 1) * ws2 + bl[2]);
;                     const f32x2 a67 = swiglu4_2(__builtin_shufflevector(g1, g1, 2, 3) * ws2 + bg[3], __builtin_shufflevector(l1, l1, 2, 3) * ws2 + bl[3]);
;                     w2[mm].x = pk4_fp8n(a01[0], a01[1], a23[0], a23[1]); w2[mm].y = pk4_fp8n(a45[0], a45[1], a67[0], a67[1]); }
;                 const u32x4 w = pair16(w2[0], w2[1]);
;                 *(u32x4*)(ACT + (size_t)(row0 + ai * HALF + (2 * mp + (fq & 1)) * 16) * FF + (f0 - 8 * (fq & 1))) = w; }
	v_pk_fma_f32 v[18:19], v[18:19], 4.0, 4.0 op_sel_hi:[1,0,0]
	v_med3_f32 v20, v20, s69, v167
	v_pk_mul_f32 v[22:23], v[18:19], v[22:23]
	v_pk_add_f32 v[18:19], v[32:33], 1.0 op_sel_hi:[1,0]
	v_med3_f32 v21, v21, s69, v167
	v_rcp_f32_e32 v18, v18
	v_rcp_f32_e32 v19, v19
	v_pk_fma_f32 v[20:21], v[20:21], 4.0, 4.0 op_sel_hi:[1,0,0]
	v_pk_mul_f32 v[24:25], v[24:25], v[18:19]
	v_mov_b32_e32 v19, v147
	v_cvt_pk_fp8_f32 v19, v22, v23
	v_pk_mul_f32 v[20:21], v[20:21], v[24:25]
	v_mov_b32_e32 v18, v147
	v_cvt_pk_fp8_f32 v18, v26, v27
	v_cvt_pk_fp8_f32 v19, v20, v21 op_sel:[0,0,1]
	v_mul_f32_e32 v20, 0x3d000000, v35
	v_pk_fma_f32 v[14:15], v[14:15], v[20:21], v[156:157] op_sel_hi:[1,0,1]
	v_pk_fma_f32 v[16:17], v[16:17], v[20:21], v[154:155] op_sel_hi:[1,0,1]
	v_min_f32_e32 v14, 0x40e00000, v14
	v_min_f32_e32 v15, 0x40e00000, v15
	v_pk_mul_f32 v[22:23], v[14:15], s[84:85] op_sel_hi:[1,0]
	v_min_f32_e32 v16, 0x40e00000, v16
	v_exp_f32_e32 v22, v22
	v_exp_f32_e32 v23, v23
	v_min_f32_e32 v17, 0x40e00000, v17
	v_pk_mul_f32 v[24:25], v[16:17], s[84:85] op_sel_hi:[1,0]
	v_pk_fma_f32 v[10:11], v[10:11], v[20:21], v[132:133] op_sel_hi:[1,0,1]
	v_pk_add_f32 v[22:23], v[22:23], 1.0 op_sel_hi:[1,0]
	v_exp_f32_e32 v24, v24
	v_rcp_f32_e32 v22, v22
	v_rcp_f32_e32 v23, v23
	v_exp_f32_e32 v25, v25
	v_med3_f32 v10, v10, s69, v167
	v_med3_f32 v11, v11, s69, v167
	v_pk_mul_f32 v[14:15], v[14:15], v[22:23]
	v_pk_fma_f32 v[10:11], v[10:11], 4.0, 4.0 op_sel_hi:[1,0,0]
	v_pk_fma_f32 v[12:13], v[12:13], v[20:21], v[128:129] op_sel_hi:[1,0,1]
	v_pk_mul_f32 v[10:11], v[10:11], v[14:15]
	v_pk_add_f32 v[14:15], v[24:25], 1.0 op_sel_hi:[1,0]
	v_med3_f32 v12, v12, s69, v167
	v_rcp_f32_e32 v14, v14
	v_rcp_f32_e32 v15, v15
	v_med3_f32 v13, v13, s69, v167
	v_pk_fma_f32 v[6:7], v[6:7], v[20:21], v[152:153] op_sel_hi:[1,0,1]
	v_pk_fma_f32 v[12:13], v[12:13], 4.0, 4.0 op_sel_hi:[1,0,0]
	v_pk_mul_f32 v[14:15], v[16:17], v[14:15]
	v_min_f32_e32 v6, 0x40e00000, v6
	v_min_f32_e32 v7, 0x40e00000, v7
	v_pk_mul_f32 v[12:13], v[12:13], v[14:15]
	v_pk_mul_f32 v[14:15], v[6:7], s[84:85] op_sel_hi:[1,0]
	v_pk_fma_f32 v[8:9], v[8:9], v[20:21], v[150:151] op_sel_hi:[1,0,1]
	v_exp_f32_e32 v14, v14
	v_exp_f32_e32 v15, v15
	v_min_f32_e32 v8, 0x40e00000, v8
	v_min_f32_e32 v9, 0x40e00000, v9
	v_pk_mul_f32 v[16:17], v[8:9], s[84:85] op_sel_hi:[1,0]
	v_pk_add_f32 v[14:15], v[14:15], 1.0 op_sel_hi:[1,0]
	v_exp_f32_e32 v16, v16
	v_rcp_f32_e32 v14, v14
	v_rcp_f32_e32 v15, v15
	v_exp_f32_e32 v17, v17
	v_pk_fma_f32 v[2:3], v[2:3], v[20:21], v[120:121] op_sel_hi:[1,0,1]
	v_pk_fma_f32 v[4:5], v[4:5], v[20:21], v[112:113] op_sel_hi:[1,0,1]
	v_med3_f32 v2, v2, s69, v167
	v_med3_f32 v3, v3, s69, v167
	v_pk_mul_f32 v[6:7], v[6:7], v[14:15]
	v_pk_fma_f32 v[2:3], v[2:3], 4.0, 4.0 op_sel_hi:[1,0,0]
	v_mov_b32_e32 v20, v147
	v_pk_mul_f32 v[2:3], v[2:3], v[6:7]
	v_pk_add_f32 v[6:7], v[16:17], 1.0 op_sel_hi:[1,0]
	v_mov_b32_e32 v21, v147
	v_rcp_f32_e32 v6, v6
	v_rcp_f32_e32 v7, v7
	v_cvt_pk_fp8_f32 v20, v10, v11
	v_cvt_pk_fp8_f32 v21, v2, v3
	v_med3_f32 v4, v4, s69, v167
	v_med3_f32 v5, v5, s69, v167
	v_pk_mul_f32 v[6:7], v[8:9], v[6:7]
	v_pk_fma_f32 v[2:3], v[4:5], 4.0, 4.0 op_sel_hi:[1,0,0]
	v_cvt_pk_fp8_f32 v18, v28, v29 op_sel:[0,0,1]
	v_pk_mul_f32 v[2:3], v[2:3], v[6:7]
	v_cvt_pk_fp8_f32 v20, v12, v13 op_sel:[0,0,1]
	v_cvt_pk_fp8_f32 v21, v2, v3 op_sel:[0,0,1]
	v_add_u32_e32 v2, 0xa0, v118
	v_ashrrev_i32_e32 v3, 31, v2
	v_lshlrev_b64 v[2:3], 11, v[2:3]
	v_lshl_add_u64 v[2:3], s[86:87], 0, v[2:3]
	v_permlane16_swap_b32_e32 v18, v20
	v_permlane16_swap_b32_e32 v19, v21
	v_lshl_add_u64 v[2:3], v[2:3], 0, v[110:111]
	global_store_dwordx4 v[2:3], v[18:21], off
	s_cbranch_vccnz .LBB0_1076
	s_lshl_b32 s0, s71, 8
	s_ashr_i32 s1, s0, 31
	v_mov_b32_e32 v2, v224
	s_lshl_b64 s[0:1], s[0:1], 2
	s_add_u32 s0, s62, s0
	v_ashrrev_i32_e32 v3, 31, v2
	s_addc_u32 s1, s63, s1
	v_lshlrev_b64 v[2:3], 2, v[2:3]
	s_mov_b32 m0, s35
	v_lshl_add_u64 v[4:5], s[0:1], 0, v[2:3]
	s_lshl_b64 s[0:1], s[30:31], 14
	v_readlane_b32 s16, v254, 25
	global_load_lds_dword v[4:5], off
	s_add_i32 m0, s35, 0x100
	v_readlane_b32 s30, v254, 39
	v_readlane_b32 s31, v254, 40
	s_add_u32 s2, s30, s0
	s_addc_u32 s3, s31, s1
	s_lshl_b32 s0, s76, 8
	s_or_b32 s0, s0, s51
	s_ashr_i32 s1, s0, 31
	s_lshl_b64 s[0:1], s[0:1], 2
	s_add_u32 s0, s2, s0
	v_lshl_add_u64 v[4:5], v[4:5], 0, s[12:13]
	s_addc_u32 s1, s3, s1
	global_load_lds_dword v[4:5], off
	v_lshl_add_u64 v[2:3], s[0:1], 0, v[2:3]
	s_mov_b32 m0, s70
	s_andn2_b64 vcc, exec, s[14:15]
	global_load_lds_dword v[2:3], off
	v_readlane_b32 s17, v254, 26
	v_readlane_b32 s18, v254, 27
	v_readlane_b32 s19, v254, 28
	v_readlane_b32 s20, v254, 29
	v_readlane_b32 s21, v254, 30
	v_readlane_b32 s22, v254, 31
	v_readlane_b32 s23, v254, 32
	v_readlane_b32 s24, v254, 33
	v_readlane_b32 s25, v254, 34
	v_readlane_b32 s26, v254, 35
	v_readlane_b32 s27, v254, 36
	v_readlane_b32 s28, v254, 37
	v_readlane_b32 s29, v254, 38
	s_cbranch_vccnz .LBB0_1075
	s_barrier
	s_branch .LBB0_1075
